# phase 6 logits loop hand-scheduled: 8 k-steps unrolled, 4-step ring of load registers, SGPR-base addressing, padded router columns not loaded
# baseline (speedup 1.0000x reference)
; __device__ __forceinline__ void phase_router(const Args& a, unsigned char* lds_g, int tid, int lane, int wave) {
;     ...
;     for (int tp = blockIdx.x; tp < NLAT / 32; tp += gridDim.x) {
;         const int tok0 = 32 * tp + 16 * slot, b = tok0 >> 11, kbase = wave * 256 + 8 * gq;
;         const bf16* xr0 = X1 + (size_t)(32 * tp + i) * D + kbase; const bf16* xr1 = xr0 + (size_t)16 * D;
;         const bf16* wh = WRh + ((size_t)(b * 48 + i) * 2048 + kbase); const bf16* wl = WRl + ((size_t)(b * 48 + i) * 2048 + kbase);
;         f32x4 ac[2][3]; float sq0 = 0.f, sq1 = 0.f;
; #pragma unroll
;         for (int s = 0; s < 2; ++s)
; #pragma unroll
;             for (int cb = 0; cb < 3; ++cb) ac[s][cb] = (f32x4){0.f, 0.f, 0.f, 0.f};
; #pragma unroll 4
;         for (int s8 = 0; s8 < 8; ++s8) {
;             const v4u xb0 = *(const v4u*)(xr0 + 32 * s8), xb1 = *(const v4u*)(xr1 + 32 * s8);
;             const bf16x8_t h0 = *(const bf16x8_t*)(wh + 32 * s8), h1 = *(const bf16x8_t*)(wh + 16 * 2048 + 32 * s8), h2 = *(const bf16x8_t*)(wh + 32 * 2048 + 32 * s8);
;             const bf16x8_t l0 = *(const bf16x8_t*)(wl + 32 * s8), l1 = *(const bf16x8_t*)(wl + 16 * 2048 + 32 * s8), l2 = *(const bf16x8_t*)(wl + 32 * 2048 + 32 * s8);
;             const bf16x8_t xf0 = __builtin_bit_cast(bf16x8_t, xb0), xf1 = __builtin_bit_cast(bf16x8_t, xb1);
;             ac[0][0] = __builtin_amdgcn_mfma_f32_16x16x32_bf16(xf0, h0, ac[0][0], 0, 0, 0); ac[0][1] = __builtin_amdgcn_mfma_f32_16x16x32_bf16(xf0, h1, ac[0][1], 0, 0, 0); ac[0][2] = __builtin_amdgcn_mfma_f32_16x16x32_bf16(xf0, h2, ac[0][2], 0, 0, 0);
;             ac[1][0] = __builtin_amdgcn_mfma_f32_16x16x32_bf16(xf1, h0, ac[1][0], 0, 0, 0); ac[1][1] = __builtin_amdgcn_mfma_f32_16x16x32_bf16(xf1, h1, ac[1][1], 0, 0, 0); ac[1][2] = __builtin_amdgcn_mfma_f32_16x16x32_bf16(xf1, h2, ac[1][2], 0, 0, 0);
;             ac[0][0] = __builtin_amdgcn_mfma_f32_16x16x32_bf16(xf0, l0, ac[0][0], 0, 0, 0); ac[0][1] = __builtin_amdgcn_mfma_f32_16x16x32_bf16(xf0, l1, ac[0][1], 0, 0, 0); ac[0][2] = __builtin_amdgcn_mfma_f32_16x16x32_bf16(xf0, l2, ac[0][2], 0, 0, 0);
;             ac[1][0] = __builtin_amdgcn_mfma_f32_16x16x32_bf16(xf1, l0, ac[1][0], 0, 0, 0); ac[1][1] = __builtin_amdgcn_mfma_f32_16x16x32_bf16(xf1, l1, ac[1][1], 0, 0, 0); ac[1][2] = __builtin_amdgcn_mfma_f32_16x16x32_bf16(xf1, l2, ac[1][2], 0, 0, 0);
.LBB0_975:
	s_lshl_b32 s31, s55, 5
	s_add_i32 s56, s31, s36
	s_ashr_i32 s30, s56, 11
	s_mul_i32 s4, s30, 48
	v_ashrrev_i32_e32 v107, 31, v106
	s_waitcnt vmcnt(0)
	v_or_b32_e32 v24, s4, v174
	v_lshlrev_b64 v[0:1], 12, v[106:107]
	v_ashrrev_i32_e32 v25, 31, v24
	v_lshl_add_u64 v[26:27], v[104:105], 0, v[0:1]
	v_lshlrev_b64 v[0:1], 12, v[24:25]
	s_mul_i32 s4, s30, 0x30000
	s_add_i32 s4, s4, s100
	v_lshl_add_u32 v0, v62, 2, s4
	v_mov_b32_e32 v1, 0
	v_lshl_add_u64 v[28:29], v[0:1], 0, s[84:85]
	s_mov_b64 s[4:5], 0
	v_mov_b32_e32 v0, 0
	v_mov_b32_e32 v1, v61
	v_mov_b32_e32 v2, v61
	v_mov_b32_e32 v3, v61
	v_mov_b32_e32 v4, 0
	v_mov_b32_e32 v5, v61
	v_mov_b32_e32 v6, v61
	v_mov_b32_e32 v7, v61
	v_mov_b32_e32 v8, 0
	v_mov_b32_e32 v9, v61
	v_mov_b32_e32 v10, v61
	v_mov_b32_e32 v11, v61
	v_mov_b32_e32 v12, 0
	v_mov_b32_e32 v13, v61
	v_mov_b32_e32 v14, v61
	v_mov_b32_e32 v15, v61
	v_mov_b32_e32 v16, 0
	v_mov_b32_e32 v17, v61
	v_mov_b32_e32 v18, v61
	v_mov_b32_e32 v19, v61
	v_mov_b32_e32 v20, 0
	v_mov_b32_e32 v21, v61
	v_mov_b32_e32 v22, v61
	v_mov_b32_e32 v23, v61
	v_mov_b32_e32 v30, 0
	v_mov_b32_e32 v31, v61
	s_add_u32 s60, s84, 0x2ea00000
	s_addc_u32 s61, s85, 0
	s_add_u32 s62, s84, 0x2ea10000
	s_addc_u32 s63, s85, 0
	s_add_u32 s64, s84, 0x601000
	s_addc_u32 s65, s85, 0
	s_add_u32 s66, s84, 0x611000
	s_addc_u32 s67, s85, 0
	s_add_u32 s68, s84, 0x621000
	s_addc_u32 s69, s85, 0
	s_add_u32 s70, s84, 0x6c1000
	s_addc_u32 s71, s85, 0
	s_add_u32 s72, s84, 0x6d1000
	s_addc_u32 s73, s85, 0
	s_add_u32 s74, s84, 0x6e1000
	s_addc_u32 s75, s85, 0
	s_mov_b32 s8, 0xf000f
	s_mov_b32 s9, 0xf000f
	v_lshlrev_b32_e32 v244, 12, v106
	s_lshr_b32 s4, s100, 4
	v_and_b32_e32 v245, 0xc0, v62
	v_lshrrev_b32_e32 v245, 2, v245
	v_or3_b32 v244, v244, s4, v245
	s_mul_i32 s4, s30, 0x30000
	s_add_i32 s4, s4, s100
	v_lshl_add_u32 v245, v62, 2, s4
	v_mov_b32_e32 v240, 0
	v_mov_b32_e32 v241, 0
	v_mov_b32_e32 v242, 0
	v_mov_b32_e32 v243, 0
	global_load_dwordx4 v[32:35], v244, s[60:61]
	global_load_dwordx4 v[36:39], v244, s[62:63]
	global_load_dwordx4 v[40:43], v245, s[64:65] offset:-4096
	global_load_dwordx4 v[44:47], v245, s[66:67] offset:-4096
	s_mov_b64 exec, s[8:9]
	global_load_dwordx4 v[48:51], v245, s[68:69] offset:-4096
	s_mov_b64 exec, -1
	global_load_dwordx4 v[52:55], v245, s[70:71] offset:-4096
	global_load_dwordx4 v[56:59], v245, s[72:73] offset:-4096
	s_mov_b64 exec, s[8:9]
	global_load_dwordx4 v[216:219], v245, s[74:75] offset:-4096
	s_mov_b64 exec, -1
	global_load_dwordx4 v[114:117], v244, s[60:61] offset:64
	global_load_dwordx4 v[118:121], v244, s[62:63] offset:64
	global_load_dwordx4 v[122:125], v245, s[64:65] offset:-3072
	global_load_dwordx4 v[126:129], v245, s[66:67] offset:-3072
	s_mov_b64 exec, s[8:9]
	global_load_dwordx4 v[130:133], v245, s[68:69] offset:-3072
	s_mov_b64 exec, -1
	global_load_dwordx4 v[134:137], v245, s[70:71] offset:-3072
	global_load_dwordx4 v[138:141], v245, s[72:73] offset:-3072
	s_mov_b64 exec, s[8:9]
	global_load_dwordx4 v[142:145], v245, s[74:75] offset:-3072
	s_mov_b64 exec, -1
	global_load_dwordx4 v[146:149], v244, s[60:61] offset:128
	global_load_dwordx4 v[150:153], v244, s[62:63] offset:128
	global_load_dwordx4 v[154:157], v245, s[64:65] offset:-2048
	global_load_dwordx4 v[158:161], v245, s[66:67] offset:-2048
	s_mov_b64 exec, s[8:9]
	global_load_dwordx4 v[162:165], v245, s[68:69] offset:-2048
	s_mov_b64 exec, -1
	global_load_dwordx4 v[166:169], v245, s[70:71] offset:-2048
	global_load_dwordx4 v[170:173], v245, s[72:73] offset:-2048
	s_mov_b64 exec, s[8:9]
	global_load_dwordx4 v[220:223], v245, s[74:75] offset:-2048
	s_mov_b64 exec, -1
	global_load_dwordx4 v[194:197], v244, s[60:61] offset:192
	global_load_dwordx4 v[198:201], v244, s[62:63] offset:192
	global_load_dwordx4 v[202:205], v245, s[64:65] offset:-1024
	global_load_dwordx4 v[206:209], v245, s[66:67] offset:-1024
	s_mov_b64 exec, s[8:9]
	global_load_dwordx4 v[210:213], v245, s[68:69] offset:-1024
	s_mov_b64 exec, -1
	global_load_dwordx4 v[224:227], v245, s[70:71] offset:-1024
	global_load_dwordx4 v[228:231], v245, s[72:73] offset:-1024
	s_mov_b64 exec, s[8:9]
	global_load_dwordx4 v[232:235], v245, s[74:75] offset:-1024
	s_mov_b64 exec, -1
	s_waitcnt vmcnt(24)
	v_mfma_f32_16x16x32_bf16 v[0:3], v[32:35], v[40:43], v[0:3]
	v_lshlrev_b32_e32 v214, 16, v32
	v_and_b32_e32 v215, 0xffff0000, v32
	v_pk_fma_f32 v[240:241], v[214:215], v[214:215], v[240:241]
	v_mfma_f32_16x16x32_bf16 v[8:11], v[32:35], v[48:51], v[8:11]
	v_lshlrev_b32_e32 v214, 16, v33
	v_and_b32_e32 v215, 0xffff0000, v33
	v_pk_fma_f32 v[240:241], v[214:215], v[214:215], v[240:241]
	v_mfma_f32_16x16x32_bf16 v[4:7], v[32:35], v[44:47], v[4:7]
	v_lshlrev_b32_e32 v214, 16, v34
	v_and_b32_e32 v215, 0xffff0000, v34
	v_pk_fma_f32 v[240:241], v[214:215], v[214:215], v[240:241]
	v_mfma_f32_16x16x32_bf16 v[16:19], v[36:39], v[44:47], v[16:19]
	v_lshlrev_b32_e32 v214, 16, v35
	v_and_b32_e32 v215, 0xffff0000, v35
	v_pk_fma_f32 v[240:241], v[214:215], v[214:215], v[240:241]
	v_mfma_f32_16x16x32_bf16 v[12:15], v[36:39], v[40:43], v[12:15]
	v_lshlrev_b32_e32 v214, 16, v36
	v_and_b32_e32 v215, 0xffff0000, v36
	v_pk_fma_f32 v[242:243], v[214:215], v[214:215], v[242:243]
	v_mfma_f32_16x16x32_bf16 v[20:23], v[36:39], v[48:51], v[20:23]
	v_lshlrev_b32_e32 v214, 16, v37
	v_and_b32_e32 v215, 0xffff0000, v37
	v_pk_fma_f32 v[242:243], v[214:215], v[214:215], v[242:243]
	v_mfma_f32_16x16x32_bf16 v[0:3], v[32:35], v[52:55], v[0:3]
	v_lshlrev_b32_e32 v214, 16, v38
	v_and_b32_e32 v215, 0xffff0000, v38
	v_pk_fma_f32 v[242:243], v[214:215], v[214:215], v[242:243]
	v_mfma_f32_16x16x32_bf16 v[8:11], v[32:35], v[216:219], v[8:11]
	v_lshlrev_b32_e32 v214, 16, v39
	v_and_b32_e32 v215, 0xffff0000, v39
	v_pk_fma_f32 v[242:243], v[214:215], v[214:215], v[242:243]
	v_mfma_f32_16x16x32_bf16 v[4:7], v[32:35], v[56:59], v[4:7]
	v_mfma_f32_16x16x32_bf16 v[16:19], v[36:39], v[56:59], v[16:19]
	v_mfma_f32_16x16x32_bf16 v[12:15], v[36:39], v[52:55], v[12:15]
	v_mfma_f32_16x16x32_bf16 v[20:23], v[36:39], v[216:219], v[20:23]
	global_load_dwordx4 v[32:35], v244, s[60:61] offset:256
	global_load_dwordx4 v[36:39], v244, s[62:63] offset:256
	global_load_dwordx4 v[40:43], v245, s[64:65]
	global_load_dwordx4 v[44:47], v245, s[66:67]
	s_mov_b64 exec, s[8:9]
	global_load_dwordx4 v[48:51], v245, s[68:69]
	s_mov_b64 exec, -1
	global_load_dwordx4 v[52:55], v245, s[70:71]
	global_load_dwordx4 v[56:59], v245, s[72:73]
	s_mov_b64 exec, s[8:9]
	global_load_dwordx4 v[216:219], v245, s[74:75]
	s_mov_b64 exec, -1
	s_waitcnt vmcnt(24)
; __device__ __forceinline__ void phase_router(const Args& a, unsigned char* lds_g, int tid, int lane, int wave) {
;     ...
;         for (int s8 = 0; s8 < 8; ++s8) {
;             const v4u xb0 = *(const v4u*)(xr0 + 32 * s8), xb1 = *(const v4u*)(xr1 + 32 * s8);
;             const bf16x8_t h0 = *(const bf16x8_t*)(wh + 32 * s8), h1 = *(const bf16x8_t*)(wh + 16 * 2048 + 32 * s8), h2 = *(const bf16x8_t*)(wh + 32 * 2048 + 32 * s8);
;             const bf16x8_t l0 = *(const bf16x8_t*)(wl + 32 * s8), l1 = *(const bf16x8_t*)(wl + 16 * 2048 + 32 * s8), l2 = *(const bf16x8_t*)(wl + 32 * 2048 + 32 * s8);
;             const bf16x8_t xf0 = __builtin_bit_cast(bf16x8_t, xb0), xf1 = __builtin_bit_cast(bf16x8_t, xb1);
;             ac[0][0] = __builtin_amdgcn_mfma_f32_16x16x32_bf16(xf0, h0, ac[0][0], 0, 0, 0); ac[0][1] = __builtin_amdgcn_mfma_f32_16x16x32_bf16(xf0, h1, ac[0][1], 0, 0, 0); ac[0][2] = __builtin_amdgcn_mfma_f32_16x16x32_bf16(xf0, h2, ac[0][2], 0, 0, 0);
;             ac[1][0] = __builtin_amdgcn_mfma_f32_16x16x32_bf16(xf1, h0, ac[1][0], 0, 0, 0); ac[1][1] = __builtin_amdgcn_mfma_f32_16x16x32_bf16(xf1, h1, ac[1][1], 0, 0, 0); ac[1][2] = __builtin_amdgcn_mfma_f32_16x16x32_bf16(xf1, h2, ac[1][2], 0, 0, 0);
;             ac[0][0] = __builtin_amdgcn_mfma_f32_16x16x32_bf16(xf0, l0, ac[0][0], 0, 0, 0); ac[0][1] = __builtin_amdgcn_mfma_f32_16x16x32_bf16(xf0, l1, ac[0][1], 0, 0, 0); ac[0][2] = __builtin_amdgcn_mfma_f32_16x16x32_bf16(xf0, l2, ac[0][2], 0, 0, 0);
;             ac[1][0] = __builtin_amdgcn_mfma_f32_16x16x32_bf16(xf1, l0, ac[1][0], 0, 0, 0); ac[1][1] = __builtin_amdgcn_mfma_f32_16x16x32_bf16(xf1, l1, ac[1][1], 0, 0, 0); ac[1][2] = __builtin_amdgcn_mfma_f32_16x16x32_bf16(xf1, l2, ac[1][2], 0, 0, 0);
;             const unsigned xw0[4] = {xb0.x, xb0.y, xb0.z, xb0.w}, xw1[4] = {xb1.x, xb1.y, xb1.z, xb1.w};
; #pragma unroll
;             for (int e = 0; e < 4; ++e) { sq0 += bflo(xw0[e]) * bflo(xw0[e]) + bfhi(xw0[e]) * bfhi(xw0[e]); sq1 += bflo(xw1[e]) * bflo(xw1[e]) + bfhi(xw1[e]) * bfhi(xw1[e]); }
;         }
	v_mfma_f32_16x16x32_bf16 v[0:3], v[114:117], v[122:125], v[0:3]
	v_lshlrev_b32_e32 v214, 16, v114
	v_and_b32_e32 v215, 0xffff0000, v114
	v_pk_fma_f32 v[240:241], v[214:215], v[214:215], v[240:241]
	v_mfma_f32_16x16x32_bf16 v[8:11], v[114:117], v[130:133], v[8:11]
	v_lshlrev_b32_e32 v214, 16, v115
	v_and_b32_e32 v215, 0xffff0000, v115
	v_pk_fma_f32 v[240:241], v[214:215], v[214:215], v[240:241]
	v_mfma_f32_16x16x32_bf16 v[4:7], v[114:117], v[126:129], v[4:7]
	v_lshlrev_b32_e32 v214, 16, v116
	v_and_b32_e32 v215, 0xffff0000, v116
	v_pk_fma_f32 v[240:241], v[214:215], v[214:215], v[240:241]
	v_mfma_f32_16x16x32_bf16 v[16:19], v[118:121], v[126:129], v[16:19]
	v_lshlrev_b32_e32 v214, 16, v117
	v_and_b32_e32 v215, 0xffff0000, v117
	v_pk_fma_f32 v[240:241], v[214:215], v[214:215], v[240:241]
	v_mfma_f32_16x16x32_bf16 v[12:15], v[118:121], v[122:125], v[12:15]
	v_lshlrev_b32_e32 v214, 16, v118
	v_and_b32_e32 v215, 0xffff0000, v118
	v_pk_fma_f32 v[242:243], v[214:215], v[214:215], v[242:243]
	v_mfma_f32_16x16x32_bf16 v[20:23], v[118:121], v[130:133], v[20:23]
	v_lshlrev_b32_e32 v214, 16, v119
	v_and_b32_e32 v215, 0xffff0000, v119
	v_pk_fma_f32 v[242:243], v[214:215], v[214:215], v[242:243]
	v_mfma_f32_16x16x32_bf16 v[0:3], v[114:117], v[134:137], v[0:3]
	v_lshlrev_b32_e32 v214, 16, v120
	v_and_b32_e32 v215, 0xffff0000, v120
	v_pk_fma_f32 v[242:243], v[214:215], v[214:215], v[242:243]
	v_mfma_f32_16x16x32_bf16 v[8:11], v[114:117], v[142:145], v[8:11]
	v_lshlrev_b32_e32 v214, 16, v121
	v_and_b32_e32 v215, 0xffff0000, v121
	v_pk_fma_f32 v[242:243], v[214:215], v[214:215], v[242:243]
	v_mfma_f32_16x16x32_bf16 v[4:7], v[114:117], v[138:141], v[4:7]
	v_mfma_f32_16x16x32_bf16 v[16:19], v[118:121], v[138:141], v[16:19]
	v_mfma_f32_16x16x32_bf16 v[12:15], v[118:121], v[134:137], v[12:15]
	v_mfma_f32_16x16x32_bf16 v[20:23], v[118:121], v[142:145], v[20:23]
	global_load_dwordx4 v[114:117], v244, s[60:61] offset:320
	global_load_dwordx4 v[118:121], v244, s[62:63] offset:320
	global_load_dwordx4 v[122:125], v245, s[64:65] offset:1024
	global_load_dwordx4 v[126:129], v245, s[66:67] offset:1024
	s_mov_b64 exec, s[8:9]
	global_load_dwordx4 v[130:133], v245, s[68:69] offset:1024
	s_mov_b64 exec, -1
	global_load_dwordx4 v[134:137], v245, s[70:71] offset:1024
	global_load_dwordx4 v[138:141], v245, s[72:73] offset:1024
	s_mov_b64 exec, s[8:9]
	global_load_dwordx4 v[142:145], v245, s[74:75] offset:1024
	s_mov_b64 exec, -1
	s_waitcnt vmcnt(24)
	v_mfma_f32_16x16x32_bf16 v[0:3], v[146:149], v[154:157], v[0:3]
	v_lshlrev_b32_e32 v214, 16, v146
	v_and_b32_e32 v215, 0xffff0000, v146
	v_pk_fma_f32 v[240:241], v[214:215], v[214:215], v[240:241]
	v_mfma_f32_16x16x32_bf16 v[8:11], v[146:149], v[162:165], v[8:11]
	v_lshlrev_b32_e32 v214, 16, v147
	v_and_b32_e32 v215, 0xffff0000, v147
	v_pk_fma_f32 v[240:241], v[214:215], v[214:215], v[240:241]
	v_mfma_f32_16x16x32_bf16 v[4:7], v[146:149], v[158:161], v[4:7]
	v_lshlrev_b32_e32 v214, 16, v148
	v_and_b32_e32 v215, 0xffff0000, v148
	v_pk_fma_f32 v[240:241], v[214:215], v[214:215], v[240:241]
	v_mfma_f32_16x16x32_bf16 v[16:19], v[150:153], v[158:161], v[16:19]
	v_lshlrev_b32_e32 v214, 16, v149
	v_and_b32_e32 v215, 0xffff0000, v149
	v_pk_fma_f32 v[240:241], v[214:215], v[214:215], v[240:241]
	v_mfma_f32_16x16x32_bf16 v[12:15], v[150:153], v[154:157], v[12:15]
	v_lshlrev_b32_e32 v214, 16, v150
	v_and_b32_e32 v215, 0xffff0000, v150
	v_pk_fma_f32 v[242:243], v[214:215], v[214:215], v[242:243]
	v_mfma_f32_16x16x32_bf16 v[20:23], v[150:153], v[162:165], v[20:23]
	v_lshlrev_b32_e32 v214, 16, v151
	v_and_b32_e32 v215, 0xffff0000, v151
	v_pk_fma_f32 v[242:243], v[214:215], v[214:215], v[242:243]
	v_mfma_f32_16x16x32_bf16 v[0:3], v[146:149], v[166:169], v[0:3]
	v_lshlrev_b32_e32 v214, 16, v152
	v_and_b32_e32 v215, 0xffff0000, v152
	v_pk_fma_f32 v[242:243], v[214:215], v[214:215], v[242:243]
	v_mfma_f32_16x16x32_bf16 v[8:11], v[146:149], v[220:223], v[8:11]
	v_lshlrev_b32_e32 v214, 16, v153
	v_and_b32_e32 v215, 0xffff0000, v153
	v_pk_fma_f32 v[242:243], v[214:215], v[214:215], v[242:243]
	v_mfma_f32_16x16x32_bf16 v[4:7], v[146:149], v[170:173], v[4:7]
	v_mfma_f32_16x16x32_bf16 v[16:19], v[150:153], v[170:173], v[16:19]
	v_mfma_f32_16x16x32_bf16 v[12:15], v[150:153], v[166:169], v[12:15]
	v_mfma_f32_16x16x32_bf16 v[20:23], v[150:153], v[220:223], v[20:23]
	global_load_dwordx4 v[146:149], v244, s[60:61] offset:384
	global_load_dwordx4 v[150:153], v244, s[62:63] offset:384
	global_load_dwordx4 v[154:157], v245, s[64:65] offset:2048
	global_load_dwordx4 v[158:161], v245, s[66:67] offset:2048
	s_mov_b64 exec, s[8:9]
	global_load_dwordx4 v[162:165], v245, s[68:69] offset:2048
	s_mov_b64 exec, -1
	global_load_dwordx4 v[166:169], v245, s[70:71] offset:2048
	global_load_dwordx4 v[170:173], v245, s[72:73] offset:2048
	s_mov_b64 exec, s[8:9]
	global_load_dwordx4 v[220:223], v245, s[74:75] offset:2048
	s_mov_b64 exec, -1
	s_waitcnt vmcnt(24)
; __device__ __forceinline__ void phase_router(const Args& a, unsigned char* lds_g, int tid, int lane, int wave) {
;     ...
;         for (int s8 = 0; s8 < 8; ++s8) {
;             const v4u xb0 = *(const v4u*)(xr0 + 32 * s8), xb1 = *(const v4u*)(xr1 + 32 * s8);
;             const bf16x8_t h0 = *(const bf16x8_t*)(wh + 32 * s8), h1 = *(const bf16x8_t*)(wh + 16 * 2048 + 32 * s8), h2 = *(const bf16x8_t*)(wh + 32 * 2048 + 32 * s8);
;             const bf16x8_t l0 = *(const bf16x8_t*)(wl + 32 * s8), l1 = *(const bf16x8_t*)(wl + 16 * 2048 + 32 * s8), l2 = *(const bf16x8_t*)(wl + 32 * 2048 + 32 * s8);
;             const bf16x8_t xf0 = __builtin_bit_cast(bf16x8_t, xb0), xf1 = __builtin_bit_cast(bf16x8_t, xb1);
;             ac[0][0] = __builtin_amdgcn_mfma_f32_16x16x32_bf16(xf0, h0, ac[0][0], 0, 0, 0); ac[0][1] = __builtin_amdgcn_mfma_f32_16x16x32_bf16(xf0, h1, ac[0][1], 0, 0, 0); ac[0][2] = __builtin_amdgcn_mfma_f32_16x16x32_bf16(xf0, h2, ac[0][2], 0, 0, 0);
;             ac[1][0] = __builtin_amdgcn_mfma_f32_16x16x32_bf16(xf1, h0, ac[1][0], 0, 0, 0); ac[1][1] = __builtin_amdgcn_mfma_f32_16x16x32_bf16(xf1, h1, ac[1][1], 0, 0, 0); ac[1][2] = __builtin_amdgcn_mfma_f32_16x16x32_bf16(xf1, h2, ac[1][2], 0, 0, 0);
;             ac[0][0] = __builtin_amdgcn_mfma_f32_16x16x32_bf16(xf0, l0, ac[0][0], 0, 0, 0); ac[0][1] = __builtin_amdgcn_mfma_f32_16x16x32_bf16(xf0, l1, ac[0][1], 0, 0, 0); ac[0][2] = __builtin_amdgcn_mfma_f32_16x16x32_bf16(xf0, l2, ac[0][2], 0, 0, 0);
;             ac[1][0] = __builtin_amdgcn_mfma_f32_16x16x32_bf16(xf1, l0, ac[1][0], 0, 0, 0); ac[1][1] = __builtin_amdgcn_mfma_f32_16x16x32_bf16(xf1, l1, ac[1][1], 0, 0, 0); ac[1][2] = __builtin_amdgcn_mfma_f32_16x16x32_bf16(xf1, l2, ac[1][2], 0, 0, 0);
;             const unsigned xw0[4] = {xb0.x, xb0.y, xb0.z, xb0.w}, xw1[4] = {xb1.x, xb1.y, xb1.z, xb1.w};
; #pragma unroll
;             for (int e = 0; e < 4; ++e) { sq0 += bflo(xw0[e]) * bflo(xw0[e]) + bfhi(xw0[e]) * bfhi(xw0[e]); sq1 += bflo(xw1[e]) * bflo(xw1[e]) + bfhi(xw1[e]) * bfhi(xw1[e]); }
;         }
	v_mfma_f32_16x16x32_bf16 v[0:3], v[194:197], v[202:205], v[0:3]
	v_lshlrev_b32_e32 v214, 16, v194
	v_and_b32_e32 v215, 0xffff0000, v194
	v_pk_fma_f32 v[240:241], v[214:215], v[214:215], v[240:241]
	v_mfma_f32_16x16x32_bf16 v[8:11], v[194:197], v[210:213], v[8:11]
	v_lshlrev_b32_e32 v214, 16, v195
	v_and_b32_e32 v215, 0xffff0000, v195
	v_pk_fma_f32 v[240:241], v[214:215], v[214:215], v[240:241]
	v_mfma_f32_16x16x32_bf16 v[4:7], v[194:197], v[206:209], v[4:7]
	v_lshlrev_b32_e32 v214, 16, v196
	v_and_b32_e32 v215, 0xffff0000, v196
	v_pk_fma_f32 v[240:241], v[214:215], v[214:215], v[240:241]
	v_mfma_f32_16x16x32_bf16 v[16:19], v[198:201], v[206:209], v[16:19]
	v_lshlrev_b32_e32 v214, 16, v197
	v_and_b32_e32 v215, 0xffff0000, v197
	v_pk_fma_f32 v[240:241], v[214:215], v[214:215], v[240:241]
	v_mfma_f32_16x16x32_bf16 v[12:15], v[198:201], v[202:205], v[12:15]
	v_lshlrev_b32_e32 v214, 16, v198
	v_and_b32_e32 v215, 0xffff0000, v198
	v_pk_fma_f32 v[242:243], v[214:215], v[214:215], v[242:243]
	v_mfma_f32_16x16x32_bf16 v[20:23], v[198:201], v[210:213], v[20:23]
	v_lshlrev_b32_e32 v214, 16, v199
	v_and_b32_e32 v215, 0xffff0000, v199
	v_pk_fma_f32 v[242:243], v[214:215], v[214:215], v[242:243]
	v_mfma_f32_16x16x32_bf16 v[0:3], v[194:197], v[224:227], v[0:3]
	v_lshlrev_b32_e32 v214, 16, v200
	v_and_b32_e32 v215, 0xffff0000, v200
	v_pk_fma_f32 v[242:243], v[214:215], v[214:215], v[242:243]
	v_mfma_f32_16x16x32_bf16 v[8:11], v[194:197], v[232:235], v[8:11]
	v_lshlrev_b32_e32 v214, 16, v201
	v_and_b32_e32 v215, 0xffff0000, v201
	v_pk_fma_f32 v[242:243], v[214:215], v[214:215], v[242:243]
	v_mfma_f32_16x16x32_bf16 v[4:7], v[194:197], v[228:231], v[4:7]
	v_mfma_f32_16x16x32_bf16 v[16:19], v[198:201], v[228:231], v[16:19]
	v_mfma_f32_16x16x32_bf16 v[12:15], v[198:201], v[224:227], v[12:15]
	v_mfma_f32_16x16x32_bf16 v[20:23], v[198:201], v[232:235], v[20:23]
	global_load_dwordx4 v[194:197], v244, s[60:61] offset:448
	global_load_dwordx4 v[198:201], v244, s[62:63] offset:448
	global_load_dwordx4 v[202:205], v245, s[64:65] offset:3072
	global_load_dwordx4 v[206:209], v245, s[66:67] offset:3072
	s_mov_b64 exec, s[8:9]
	global_load_dwordx4 v[210:213], v245, s[68:69] offset:3072
	s_mov_b64 exec, -1
	global_load_dwordx4 v[224:227], v245, s[70:71] offset:3072
	global_load_dwordx4 v[228:231], v245, s[72:73] offset:3072
	s_mov_b64 exec, s[8:9]
	global_load_dwordx4 v[232:235], v245, s[74:75] offset:3072
	s_mov_b64 exec, -1
	s_waitcnt vmcnt(24)
	v_mfma_f32_16x16x32_bf16 v[0:3], v[32:35], v[40:43], v[0:3]
	v_lshlrev_b32_e32 v214, 16, v32
	v_and_b32_e32 v215, 0xffff0000, v32
	v_pk_fma_f32 v[240:241], v[214:215], v[214:215], v[240:241]
	v_mfma_f32_16x16x32_bf16 v[8:11], v[32:35], v[48:51], v[8:11]
	v_lshlrev_b32_e32 v214, 16, v33
	v_and_b32_e32 v215, 0xffff0000, v33
	v_pk_fma_f32 v[240:241], v[214:215], v[214:215], v[240:241]
	v_mfma_f32_16x16x32_bf16 v[4:7], v[32:35], v[44:47], v[4:7]
	v_lshlrev_b32_e32 v214, 16, v34
	v_and_b32_e32 v215, 0xffff0000, v34
	v_pk_fma_f32 v[240:241], v[214:215], v[214:215], v[240:241]
	v_mfma_f32_16x16x32_bf16 v[16:19], v[36:39], v[44:47], v[16:19]
	v_lshlrev_b32_e32 v214, 16, v35
	v_and_b32_e32 v215, 0xffff0000, v35
	v_pk_fma_f32 v[240:241], v[214:215], v[214:215], v[240:241]
	v_mfma_f32_16x16x32_bf16 v[12:15], v[36:39], v[40:43], v[12:15]
	v_lshlrev_b32_e32 v214, 16, v36
	v_and_b32_e32 v215, 0xffff0000, v36
	v_pk_fma_f32 v[242:243], v[214:215], v[214:215], v[242:243]
	v_mfma_f32_16x16x32_bf16 v[20:23], v[36:39], v[48:51], v[20:23]
	v_lshlrev_b32_e32 v214, 16, v37
	v_and_b32_e32 v215, 0xffff0000, v37
	v_pk_fma_f32 v[242:243], v[214:215], v[214:215], v[242:243]
	v_mfma_f32_16x16x32_bf16 v[0:3], v[32:35], v[52:55], v[0:3]
	v_lshlrev_b32_e32 v214, 16, v38
	v_and_b32_e32 v215, 0xffff0000, v38
	v_pk_fma_f32 v[242:243], v[214:215], v[214:215], v[242:243]
	v_mfma_f32_16x16x32_bf16 v[8:11], v[32:35], v[216:219], v[8:11]
	v_lshlrev_b32_e32 v214, 16, v39
	v_and_b32_e32 v215, 0xffff0000, v39
	v_pk_fma_f32 v[242:243], v[214:215], v[214:215], v[242:243]
	v_mfma_f32_16x16x32_bf16 v[4:7], v[32:35], v[56:59], v[4:7]
	v_mfma_f32_16x16x32_bf16 v[16:19], v[36:39], v[56:59], v[16:19]
	v_mfma_f32_16x16x32_bf16 v[12:15], v[36:39], v[52:55], v[12:15]
	v_mfma_f32_16x16x32_bf16 v[20:23], v[36:39], v[216:219], v[20:23]
	s_waitcnt vmcnt(16)
	v_mfma_f32_16x16x32_bf16 v[0:3], v[114:117], v[122:125], v[0:3]
	v_lshlrev_b32_e32 v214, 16, v114
	v_and_b32_e32 v215, 0xffff0000, v114
	v_pk_fma_f32 v[240:241], v[214:215], v[214:215], v[240:241]
	v_mfma_f32_16x16x32_bf16 v[8:11], v[114:117], v[130:133], v[8:11]
	v_lshlrev_b32_e32 v214, 16, v115
	v_and_b32_e32 v215, 0xffff0000, v115
	v_pk_fma_f32 v[240:241], v[214:215], v[214:215], v[240:241]
	v_mfma_f32_16x16x32_bf16 v[4:7], v[114:117], v[126:129], v[4:7]
	v_lshlrev_b32_e32 v214, 16, v116
	v_and_b32_e32 v215, 0xffff0000, v116
	v_pk_fma_f32 v[240:241], v[214:215], v[214:215], v[240:241]
	v_mfma_f32_16x16x32_bf16 v[16:19], v[118:121], v[126:129], v[16:19]
	v_lshlrev_b32_e32 v214, 16, v117
	v_and_b32_e32 v215, 0xffff0000, v117
	v_pk_fma_f32 v[240:241], v[214:215], v[214:215], v[240:241]
	v_mfma_f32_16x16x32_bf16 v[12:15], v[118:121], v[122:125], v[12:15]
	v_lshlrev_b32_e32 v214, 16, v118
	v_and_b32_e32 v215, 0xffff0000, v118
	v_pk_fma_f32 v[242:243], v[214:215], v[214:215], v[242:243]
	v_mfma_f32_16x16x32_bf16 v[20:23], v[118:121], v[130:133], v[20:23]
	v_lshlrev_b32_e32 v214, 16, v119
	v_and_b32_e32 v215, 0xffff0000, v119
	v_pk_fma_f32 v[242:243], v[214:215], v[214:215], v[242:243]
	v_mfma_f32_16x16x32_bf16 v[0:3], v[114:117], v[134:137], v[0:3]
	v_lshlrev_b32_e32 v214, 16, v120
	v_and_b32_e32 v215, 0xffff0000, v120
	v_pk_fma_f32 v[242:243], v[214:215], v[214:215], v[242:243]
	v_mfma_f32_16x16x32_bf16 v[8:11], v[114:117], v[142:145], v[8:11]
	v_lshlrev_b32_e32 v214, 16, v121
	v_and_b32_e32 v215, 0xffff0000, v121
	v_pk_fma_f32 v[242:243], v[214:215], v[214:215], v[242:243]
	v_mfma_f32_16x16x32_bf16 v[4:7], v[114:117], v[138:141], v[4:7]
	v_mfma_f32_16x16x32_bf16 v[16:19], v[118:121], v[138:141], v[16:19]
	v_mfma_f32_16x16x32_bf16 v[12:15], v[118:121], v[134:137], v[12:15]
	v_mfma_f32_16x16x32_bf16 v[20:23], v[118:121], v[142:145], v[20:23]
	s_waitcnt vmcnt(8)
; __device__ __forceinline__ void phase_router(const Args& a, unsigned char* lds_g, int tid, int lane, int wave) {
;     ...
;         for (int s8 = 0; s8 < 8; ++s8) {
;             const v4u xb0 = *(const v4u*)(xr0 + 32 * s8), xb1 = *(const v4u*)(xr1 + 32 * s8);
;             const bf16x8_t h0 = *(const bf16x8_t*)(wh + 32 * s8), h1 = *(const bf16x8_t*)(wh + 16 * 2048 + 32 * s8), h2 = *(const bf16x8_t*)(wh + 32 * 2048 + 32 * s8);
;             const bf16x8_t l0 = *(const bf16x8_t*)(wl + 32 * s8), l1 = *(const bf16x8_t*)(wl + 16 * 2048 + 32 * s8), l2 = *(const bf16x8_t*)(wl + 32 * 2048 + 32 * s8);
;             const bf16x8_t xf0 = __builtin_bit_cast(bf16x8_t, xb0), xf1 = __builtin_bit_cast(bf16x8_t, xb1);
;             ac[0][0] = __builtin_amdgcn_mfma_f32_16x16x32_bf16(xf0, h0, ac[0][0], 0, 0, 0); ac[0][1] = __builtin_amdgcn_mfma_f32_16x16x32_bf16(xf0, h1, ac[0][1], 0, 0, 0); ac[0][2] = __builtin_amdgcn_mfma_f32_16x16x32_bf16(xf0, h2, ac[0][2], 0, 0, 0);
;             ac[1][0] = __builtin_amdgcn_mfma_f32_16x16x32_bf16(xf1, h0, ac[1][0], 0, 0, 0); ac[1][1] = __builtin_amdgcn_mfma_f32_16x16x32_bf16(xf1, h1, ac[1][1], 0, 0, 0); ac[1][2] = __builtin_amdgcn_mfma_f32_16x16x32_bf16(xf1, h2, ac[1][2], 0, 0, 0);
;             ac[0][0] = __builtin_amdgcn_mfma_f32_16x16x32_bf16(xf0, l0, ac[0][0], 0, 0, 0); ac[0][1] = __builtin_amdgcn_mfma_f32_16x16x32_bf16(xf0, l1, ac[0][1], 0, 0, 0); ac[0][2] = __builtin_amdgcn_mfma_f32_16x16x32_bf16(xf0, l2, ac[0][2], 0, 0, 0);
;             ac[1][0] = __builtin_amdgcn_mfma_f32_16x16x32_bf16(xf1, l0, ac[1][0], 0, 0, 0); ac[1][1] = __builtin_amdgcn_mfma_f32_16x16x32_bf16(xf1, l1, ac[1][1], 0, 0, 0); ac[1][2] = __builtin_amdgcn_mfma_f32_16x16x32_bf16(xf1, l2, ac[1][2], 0, 0, 0);
;             const unsigned xw0[4] = {xb0.x, xb0.y, xb0.z, xb0.w}, xw1[4] = {xb1.x, xb1.y, xb1.z, xb1.w};
; #pragma unroll
;             for (int e = 0; e < 4; ++e) { sq0 += bflo(xw0[e]) * bflo(xw0[e]) + bfhi(xw0[e]) * bfhi(xw0[e]); sq1 += bflo(xw1[e]) * bflo(xw1[e]) + bfhi(xw1[e]) * bfhi(xw1[e]); }
;         }
;         sq0 += __shfl_xor(sq0, 16); sq0 += __shfl_xor(sq0, 32); sq1 += __shfl_xor(sq1, 16); sq1 += __shfl_xor(sq1, 32);
; #pragma unroll
;         for (int s = 0; s < 2; ++s)
; #pragma unroll
;             for (int cb = 0; cb < 3; ++cb) PART[((s * 8 + wave) * 3 + cb) * 64 + lane] = ac[s][cb];
	v_mfma_f32_16x16x32_bf16 v[0:3], v[146:149], v[154:157], v[0:3]
	v_lshlrev_b32_e32 v214, 16, v146
	v_and_b32_e32 v215, 0xffff0000, v146
	v_pk_fma_f32 v[240:241], v[214:215], v[214:215], v[240:241]
	v_mfma_f32_16x16x32_bf16 v[8:11], v[146:149], v[162:165], v[8:11]
	v_lshlrev_b32_e32 v214, 16, v147
	v_and_b32_e32 v215, 0xffff0000, v147
	v_pk_fma_f32 v[240:241], v[214:215], v[214:215], v[240:241]
	v_mfma_f32_16x16x32_bf16 v[4:7], v[146:149], v[158:161], v[4:7]
	v_lshlrev_b32_e32 v214, 16, v148
	v_and_b32_e32 v215, 0xffff0000, v148
	v_pk_fma_f32 v[240:241], v[214:215], v[214:215], v[240:241]
	v_mfma_f32_16x16x32_bf16 v[16:19], v[150:153], v[158:161], v[16:19]
	v_lshlrev_b32_e32 v214, 16, v149
	v_and_b32_e32 v215, 0xffff0000, v149
	v_pk_fma_f32 v[240:241], v[214:215], v[214:215], v[240:241]
	v_mfma_f32_16x16x32_bf16 v[12:15], v[150:153], v[154:157], v[12:15]
	v_lshlrev_b32_e32 v214, 16, v150
	v_and_b32_e32 v215, 0xffff0000, v150
	v_pk_fma_f32 v[242:243], v[214:215], v[214:215], v[242:243]
	v_mfma_f32_16x16x32_bf16 v[20:23], v[150:153], v[162:165], v[20:23]
	v_lshlrev_b32_e32 v214, 16, v151
	v_and_b32_e32 v215, 0xffff0000, v151
	v_pk_fma_f32 v[242:243], v[214:215], v[214:215], v[242:243]
	v_mfma_f32_16x16x32_bf16 v[0:3], v[146:149], v[166:169], v[0:3]
	v_lshlrev_b32_e32 v214, 16, v152
	v_and_b32_e32 v215, 0xffff0000, v152
	v_pk_fma_f32 v[242:243], v[214:215], v[214:215], v[242:243]
	v_mfma_f32_16x16x32_bf16 v[8:11], v[146:149], v[220:223], v[8:11]
	v_lshlrev_b32_e32 v214, 16, v153
	v_and_b32_e32 v215, 0xffff0000, v153
	v_pk_fma_f32 v[242:243], v[214:215], v[214:215], v[242:243]
	v_mfma_f32_16x16x32_bf16 v[4:7], v[146:149], v[170:173], v[4:7]
	v_mfma_f32_16x16x32_bf16 v[16:19], v[150:153], v[170:173], v[16:19]
	v_mfma_f32_16x16x32_bf16 v[12:15], v[150:153], v[166:169], v[12:15]
	v_mfma_f32_16x16x32_bf16 v[20:23], v[150:153], v[220:223], v[20:23]
	s_waitcnt vmcnt(0)
	v_mfma_f32_16x16x32_bf16 v[0:3], v[194:197], v[202:205], v[0:3]
	v_lshlrev_b32_e32 v214, 16, v194
	v_and_b32_e32 v215, 0xffff0000, v194
	v_pk_fma_f32 v[240:241], v[214:215], v[214:215], v[240:241]
	v_mfma_f32_16x16x32_bf16 v[8:11], v[194:197], v[210:213], v[8:11]
	v_lshlrev_b32_e32 v214, 16, v195
	v_and_b32_e32 v215, 0xffff0000, v195
	v_pk_fma_f32 v[240:241], v[214:215], v[214:215], v[240:241]
	v_mfma_f32_16x16x32_bf16 v[4:7], v[194:197], v[206:209], v[4:7]
	v_lshlrev_b32_e32 v214, 16, v196
	v_and_b32_e32 v215, 0xffff0000, v196
	v_pk_fma_f32 v[240:241], v[214:215], v[214:215], v[240:241]
	v_mfma_f32_16x16x32_bf16 v[16:19], v[198:201], v[206:209], v[16:19]
	v_lshlrev_b32_e32 v214, 16, v197
	v_and_b32_e32 v215, 0xffff0000, v197
	v_pk_fma_f32 v[240:241], v[214:215], v[214:215], v[240:241]
	v_mfma_f32_16x16x32_bf16 v[12:15], v[198:201], v[202:205], v[12:15]
	v_lshlrev_b32_e32 v214, 16, v198
	v_and_b32_e32 v215, 0xffff0000, v198
	v_pk_fma_f32 v[242:243], v[214:215], v[214:215], v[242:243]
	v_mfma_f32_16x16x32_bf16 v[20:23], v[198:201], v[210:213], v[20:23]
	v_lshlrev_b32_e32 v214, 16, v199
	v_and_b32_e32 v215, 0xffff0000, v199
	v_pk_fma_f32 v[242:243], v[214:215], v[214:215], v[242:243]
	v_mfma_f32_16x16x32_bf16 v[0:3], v[194:197], v[224:227], v[0:3]
	v_lshlrev_b32_e32 v214, 16, v200
	v_and_b32_e32 v215, 0xffff0000, v200
	v_pk_fma_f32 v[242:243], v[214:215], v[214:215], v[242:243]
	v_mfma_f32_16x16x32_bf16 v[8:11], v[194:197], v[232:235], v[8:11]
	v_lshlrev_b32_e32 v214, 16, v201
	v_and_b32_e32 v215, 0xffff0000, v201
	v_pk_fma_f32 v[242:243], v[214:215], v[214:215], v[242:243]
	v_mfma_f32_16x16x32_bf16 v[4:7], v[194:197], v[228:231], v[4:7]
	v_mfma_f32_16x16x32_bf16 v[16:19], v[198:201], v[228:231], v[16:19]
	v_mfma_f32_16x16x32_bf16 v[12:15], v[198:201], v[224:227], v[12:15]
	v_mfma_f32_16x16x32_bf16 v[20:23], v[198:201], v[232:235], v[20:23]
	v_add_f32_e32 v30, v240, v241
	v_add_f32_e32 v31, v242, v243
	ds_bpermute_b32 v26, v175, v30
	ds_bpermute_b32 v27, v175, v31
	v_add_u32_e32 v32, s38, v64
	ds_write_b128 v32, v[0:3]
	ds_write_b128 v32, v[4:7] offset:1024
	ds_write_b128 v32, v[8:11] offset:2048
	ds_write_b128 v32, v[12:15] offset:24576
	ds_write_b128 v32, v[16:19] offset:25600
	ds_write_b128 v32, v[20:23] offset:26624
	s_waitcnt lgkmcnt(0)
	v_add_f32_e32 v26, v30, v26
	v_add_f32_e32 v27, v31, v27
	ds_bpermute_b32 v28, v176, v26
	ds_bpermute_b32 v29, v176, v27
	s_and_saveexec_b64 s[4:5], s[0:1]
	s_cbranch_execz .LBB0_979
	s_waitcnt lgkmcnt(1)
	v_add_f32_e32 v0, v26, v28
	s_waitcnt lgkmcnt(0)
	v_add_f32_e32 v1, v27, v29
	ds_write_b32 v65, v0 offset:49152
	ds_write_b32 v177, v1 offset:49664
